# F1 + attention unit prologue (layer 0): the five global loads of key tile 1 issued right after the first barrier, before the first QK^T (latency overlaps 24 MFMAs + row max)
# baseline (speedup 1.0000x reference)
.LBB0_756:
	s_and_b32 s8, s8, 7
	s_ashr_i32 s31, s30, 31
	s_mul_i32 s7, s30, 0xc00
	s_mul_hi_i32 s6, s30, 0xc00
	s_add_u32 s7, s37, s7
	s_addc_u32 s6, s38, s6
	s_mul_i32 s9, s8, 0x180
	s_add_u32 s10, s7, s9
	s_addc_u32 s11, s6, 0
	s_add_u32 s6, s39, s9
	s_addc_u32 s7, s40, 0
	s_lshl_b32 s61, s8, 7
	s_lshl_b32 s8, s8, 8
	s_add_u32 s34, s41, s8
	v_readfirstlane_b32 s9, v254
	s_addc_u32 s35, s42, 0
	s_ashr_i32 s8, s9, 6
	s_lshl_b32 s82, s8, 10
	s_mov_b32 s72, s6
	s_and_b32 s73, s7, 0xffff
	s_mov_b32 s74, 0x7ffffff0
	s_mov_b32 s75, 0x20000
	s_mov_b32 s76, s34
	s_and_b32 s77, s35, 0xffff
	s_mov_b32 s78, 0x7ffffff0
	s_mov_b32 s79, 0x20000
	v_lshl_or_b32 v2, s8, 5, v188
	v_mov_b64_e32 v[0:1], s[10:11]
	v_mad_i64_i32 v[0:1], s[10:11], v2, s46, v[0:1]
	v_lshl_add_u64 v[26:27], s[26:27], 0, v[142:143]
	v_lshl_add_u64 v[28:29], v[146:147], 0, s[26:27]
	v_lshl_add_u64 v[38:39], v[0:1], 0, v[148:149]
	v_lshlrev_b64 v[0:1], 11, v[26:27]
	v_lshlrev_b64 v[18:19], 11, v[28:29]
	v_lshl_add_u64 v[0:1], s[34:35], 0, v[0:1]
	v_lshl_add_u64 v[18:19], s[34:35], 0, v[18:19]
	v_lshl_add_u64 v[0:1], v[0:1], 0, v[150:151]
	v_lshl_add_u64 v[22:23], v[18:19], 0, v[150:151]
	global_load_dwordx4 v[2:5], v[38:39], off offset:256
	global_load_dwordx4 v[6:9], v[38:39], off offset:288
	global_load_dwordx4 v[10:13], v[38:39], off offset:320
	global_load_dwordx4 v[14:17], v[38:39], off offset:352
	global_load_dwordx4 v[18:21], v[0:1], off
	s_nop 0
	global_load_dwordx4 v[22:25], v[22:23], off
	v_mov_b64_e32 v[0:1], s[6:7]
	v_mad_u64_u32 v[30:31], s[10:11], v26, s46, v[0:1]
	v_mad_i32_i24 v31, v27, s46, v31
	v_lshl_add_u64 v[26:27], v[30:31], 0, v[150:151]
	v_mad_u64_u32 v[30:31], s[10:11], v28, s46, v[0:1]
	v_mad_i32_i24 v31, v29, s46, v31
	v_lshl_add_u64 v[30:31], v[30:31], 0, v[150:151]
	v_lshl_add_u64 v[34:35], s[26:27], 0, v[144:145]
	global_load_dwordx4 v[26:29], v[26:27], off
	s_nop 0
	global_load_dwordx4 v[30:33], v[30:31], off
	v_mad_u64_u32 v[36:37], s[10:11], v34, s46, v[0:1]
	v_mad_i32_i24 v37, v35, s46, v37
	v_lshl_add_u64 v[34:35], v[36:37], 0, v[152:153]
	global_load_dwordx4 v[34:37], v[34:35], off offset:256
	s_nop 0
	global_load_dwordx4 v[124:127], v[38:39], off
	global_load_dwordx4 v[120:123], v[38:39], off offset:32
	global_load_dwordx4 v[116:119], v[38:39], off offset:64
	global_load_dwordx4 v[112:115], v[38:39], off offset:96
	global_load_dwordx4 v[108:111], v[38:39], off offset:128
	global_load_dwordx4 v[104:107], v[38:39], off offset:160
	global_load_dwordx4 v[100:103], v[38:39], off offset:192
	global_load_dwordx4 v[96:99], v[38:39], off offset:224
	s_lshl_b32 s8, s8, 12
	v_add_u32_e32 v190, s8, v166
	v_add_u32_e32 v191, s47, v170
	v_add_u32_e32 v192, s47, v171
	v_add_u32_e32 v193, s47, v172
	v_add_u32_e32 v194, s47, v173
	s_and_b32 s9, s9, 0x3fffffc0
	s_lshl_b32 s9, s9, 2
	s_add_i32 s62, s9, 0
	s_add_i32 s62, s62, 0x14000
	s_mov_b32 s11, s27
	s_mov_b32 s22, s27
	s_mov_b32 s23, s27
	s_mov_b32 s8, s27
	s_mov_b32 s9, s27
	s_mov_b32 s12, s27
	s_mov_b32 s13, s27
	s_mov_b32 s14, s27
	s_mov_b32 s15, s27
	s_mov_b32 s16, s27
	s_mov_b32 s17, s27
	s_mov_b32 s18, s27
	s_mov_b32 s19, s27
	s_mov_b32 s20, s27
	s_mov_b32 s21, s27
	v_add_u32_e32 v195, 0, v168
	s_mov_b32 s64, 2
	v_mov_b32_e32 v140, 0
	v_add_u32_e32 v196, 0x12000, v195
	v_lshrrev_b32_e32 v156, 4, v254
	v_and_b32_e32 v157, 15, v156
	v_and_b32_e32 v159, 15, v254
	v_xor_b32_e32 v157, v157, v159
	v_lshlrev_b32_e32 v157, 4, v157
	v_mad_u32_u24 v154, v156, s46, v157
	v_lshrrev_b32_e32 v156, 3, v254
	v_bfe_u32 v157, v254, 4, 3
	v_and_b32_e32 v159, 7, v254
	v_xor_b32_e32 v157, v157, v159
	v_lshlrev_b32_e32 v157, 4, v157
	v_add_u32_e32 v157, 0x100, v157
	v_mad_u32_u24 v155, v156, s46, v157
	v_and_b32_e32 v158, 3, v254
	v_lshlrev_b32_e32 v158, 4, v158
	v_bfe_u32 v156, v254, 5, 2
	v_lshl_or_b32 v158, v156, 6, v158
	v_bfe_u32 v156, v254, 2, 2
	v_lshl_or_b32 v158, v156, 11, v158
	v_bfe_u32 v156, v254, 7, 1
	v_lshl_or_b32 v158, v156, 13, v158
	v_bfe_u32 v156, v254, 4, 1
	v_lshl_or_b32 v158, v156, 14, v158
	v_bfe_u32 v156, v254, 8, 1
	v_lshl_or_b32 v158, v156, 15, v158
	v_lshl_add_u32 v189, v188, 2, s62
	s_waitcnt vmcnt(16)
	ds_write_b128 v190, v[2:5]
	s_waitcnt vmcnt(15)
	ds_write_b128 v190, v[6:9] offset:1024
	s_waitcnt vmcnt(14)
	ds_write_b128 v190, v[10:13] offset:2048
	s_waitcnt vmcnt(13)
	ds_write_b128 v190, v[14:17] offset:3072
	s_waitcnt vmcnt(0)
	s_waitcnt vmcnt(12)
	ds_write_b128 v175, v[18:21]
	s_waitcnt vmcnt(11)
	ds_write_b128 v176, v[22:25]
	s_waitcnt vmcnt(10)
	ds_write_b128 v177, v[26:29] offset:32768
	s_waitcnt vmcnt(9)
	ds_write_b128 v178, v[30:33] offset:32768
	s_waitcnt vmcnt(8)
	ds_write_b128 v179, v[34:37]
	s_waitcnt lgkmcnt(0)
	s_barrier
	s_add_i32 s10, s26, 64
	v_lshl_add_u64 v[2:3], s[10:11], 0, v[142:143]
	v_lshl_add_u64 v[4:5], v[146:147], 0, s[10:11]
	v_lshl_add_u64 v[6:7], s[10:11], 0, v[144:145]
	v_lshlrev_b64 v[8:9], 11, v[2:3]
	v_lshlrev_b64 v[10:11], 11, v[4:5]
	v_mad_u64_u32 v[12:13], s[10:11], v2, s46, v[0:1]
	v_mad_u64_u32 v[14:15], s[10:11], v4, s46, v[0:1]
	v_mad_u64_u32 v[0:1], s[10:11], v6, s46, v[0:1]
	v_lshl_add_u64 v[8:9], s[34:35], 0, v[8:9]
	v_lshl_add_u64 v[10:11], s[34:35], 0, v[10:11]
	v_mad_i32_i24 v13, v3, s46, v13
	v_mad_i32_i24 v15, v5, s46, v15
	v_mad_i32_i24 v1, v7, s46, v1
	v_lshl_add_u64 v[2:3], v[8:9], 0, v[150:151]
	v_lshl_add_u64 v[4:5], v[10:11], 0, v[150:151]
	v_lshl_add_u64 v[6:7], v[12:13], 0, v[150:151]
	v_lshl_add_u64 v[8:9], v[14:15], 0, v[150:151]
	v_lshl_add_u64 v[0:1], v[0:1], 0, v[152:153]
	global_load_dwordx4 v[80:83], v[2:3], off
	global_load_dwordx4 v[84:87], v[4:5], off
	global_load_dwordx4 v[88:91], v[6:7], off
	global_load_dwordx4 v[92:95], v[8:9], off
	global_load_dwordx4 v[200:203], v[0:1], off offset:256
	ds_read_b128 v[2:5], v180 offset:32768
	ds_read_b128 v[6:9], v180 offset:40960
	s_waitcnt vmcnt(12) lgkmcnt(1)
	v_mfma_f32_32x32x16_bf16 v[48:63], v[2:5], v[124:127], 0
	s_waitcnt lgkmcnt(0)
	v_mfma_f32_32x32x16_bf16 v[64:79], v[6:9], v[124:127], 0
	ds_read_b128 v[2:5], v181 offset:32768
	ds_read_b128 v[6:9], v181 offset:40960
	s_waitcnt vmcnt(11) lgkmcnt(1)
	v_mfma_f32_32x32x16_bf16 v[48:63], v[2:5], v[120:123], v[48:63]
	s_waitcnt lgkmcnt(0)
	v_mfma_f32_32x32x16_bf16 v[64:79], v[6:9], v[120:123], v[64:79]
	ds_read_b128 v[2:5], v182 offset:32768
	ds_read_b128 v[6:9], v182 offset:40960
	s_waitcnt vmcnt(10) lgkmcnt(1)
	v_mfma_f32_32x32x16_bf16 v[48:63], v[2:5], v[116:119], v[48:63]
	s_waitcnt lgkmcnt(0)
	v_mfma_f32_32x32x16_bf16 v[64:79], v[6:9], v[116:119], v[64:79]
	ds_read_b128 v[2:5], v183 offset:32768
	ds_read_b128 v[6:9], v183 offset:40960
	s_waitcnt vmcnt(9) lgkmcnt(1)
	v_mfma_f32_32x32x16_bf16 v[48:63], v[2:5], v[112:115], v[48:63]
	s_waitcnt lgkmcnt(0)
	v_mfma_f32_32x32x16_bf16 v[64:79], v[6:9], v[112:115], v[64:79]
	ds_read_b128 v[2:5], v184 offset:32768
	ds_read_b128 v[6:9], v184 offset:40960
	s_waitcnt vmcnt(8) lgkmcnt(1)
	v_mfma_f32_32x32x16_bf16 v[48:63], v[2:5], v[108:111], v[48:63]
	s_waitcnt lgkmcnt(0)
	v_mfma_f32_32x32x16_bf16 v[64:79], v[6:9], v[108:111], v[64:79]
	ds_read_b128 v[2:5], v185 offset:32768
	ds_read_b128 v[6:9], v185 offset:40960
	s_waitcnt vmcnt(7) lgkmcnt(1)
	v_mfma_f32_32x32x16_bf16 v[48:63], v[2:5], v[104:107], v[48:63]
	s_waitcnt lgkmcnt(0)
	v_mfma_f32_32x32x16_bf16 v[64:79], v[6:9], v[104:107], v[64:79]
	ds_read_b128 v[2:5], v186 offset:32768
	ds_read_b128 v[6:9], v186 offset:40960
	s_waitcnt vmcnt(6) lgkmcnt(1)
	v_mfma_f32_32x32x16_bf16 v[48:63], v[2:5], v[100:103], v[48:63]
	s_waitcnt lgkmcnt(0)
	v_mfma_f32_32x32x16_bf16 v[64:79], v[6:9], v[100:103], v[64:79]
	ds_read_b128 v[2:5], v187 offset:32768
	ds_read_b128 v[6:9], v187 offset:40960
	s_waitcnt vmcnt(5) lgkmcnt(1)
	v_mfma_f32_32x32x16_bf16 v[48:63], v[2:5], v[96:99], v[48:63]
	s_waitcnt lgkmcnt(0)
	v_mfma_f32_32x32x16_bf16 v[64:79], v[6:9], v[96:99], v[64:79]
	ds_read_b128 v[2:5], v191
	ds_read_b128 v[6:9], v190
	ds_read_b128 v[10:13], v191 offset:4096
	ds_read_b128 v[14:17], v190 offset:1024
	s_waitcnt lgkmcnt(2)
	v_mfma_f32_32x32x16_bf16 v[48:63], v[2:5], v[6:9], v[48:63]
	s_waitcnt lgkmcnt(1)
	v_mfma_f32_32x32x16_bf16 v[64:79], v[10:13], v[6:9], v[64:79]
	ds_read_b128 v[2:5], v192
	ds_read_b128 v[6:9], v192 offset:4096
	s_waitcnt lgkmcnt(1)
	v_mfma_f32_32x32x16_bf16 v[48:63], v[2:5], v[14:17], v[48:63]
	s_waitcnt lgkmcnt(0)
	v_mfma_f32_32x32x16_bf16 v[64:79], v[6:9], v[14:17], v[64:79]
	ds_read_b128 v[2:5], v193
	ds_read_b128 v[6:9], v190 offset:2048
	ds_read_b128 v[10:13], v193 offset:4096
	ds_read_b128 v[14:17], v190 offset:3072
	s_waitcnt lgkmcnt(2)
	v_mfma_f32_32x32x16_bf16 v[48:63], v[2:5], v[6:9], v[48:63]
	s_waitcnt lgkmcnt(1)
	v_mfma_f32_32x32x16_bf16 v[64:79], v[10:13], v[6:9], v[64:79]
	ds_read_b128 v[2:5], v194
	ds_read_b128 v[6:9], v194 offset:4096
	s_waitcnt lgkmcnt(1)
	v_mfma_f32_32x32x16_bf16 v[48:63], v[2:5], v[14:17], v[48:63]
	s_waitcnt lgkmcnt(0)
	v_mfma_f32_32x32x16_bf16 v[64:79], v[6:9], v[14:17], v[64:79]
	s_nop 9
	v_max_f32_e32 v2, v49, v49
	v_max_f32_e32 v3, v48, v48
	v_max_f32_e32 v2, v3, v2
	v_max3_f32 v2, v2, v50, v51
	v_max3_f32 v2, v2, v52, v53
	v_max3_f32 v2, v2, v54, v55
	v_max3_f32 v2, v2, v56, v57
	v_max3_f32 v2, v2, v58, v59
	v_max3_f32 v2, v2, v60, v61
	v_max3_f32 v2, v2, v62, v63
	v_max3_f32 v2, v2, v64, v65
	v_max3_f32 v2, v2, v66, v67
	v_max3_f32 v2, v2, v68, v69
	v_max3_f32 v2, v2, v70, v71
	v_max3_f32 v2, v2, v72, v73
	v_max3_f32 v2, v2, v74, v75
	v_max3_f32 v2, v2, v76, v77
	v_max3_f32 v2, v2, v78, v79
	v_mov_b32_e32 v3, v2
	s_nop 1
	v_permlane32_swap_b32_e32 v2, v3
	v_max_f32_e32 v3, v3, v3
	v_max_f32_e32 v2, v2, v2
	v_max_f32_e32 v2, v2, v3
	v_add_f32_e32 v3, 0x7149f2ca, v2
	v_cmp_ge_f32_e32 vcc, s48, v3
	s_cmp_eq_u64 vcc, exec
	s_cselect_b64 vcc, -1, 0
	v_max_f32_e32 v128, 0xf149f2ca, v2
	v_sub_f32_e32 v129, 0xf149f2ca, v128
	v_mul_f32_e32 v129, 0x3dd53b94, v129
	v_exp_f32_e32 v164, v129
	v_mov_b32_e32 v129, 0xf149f2ca
	v_cndmask_b32_e32 v198, v128, v129, vcc
	v_mul_f32_e32 v138, 0xbdd53b94, v198
	v_mov_b32_e32 v165, v138
	v_fmamk_f32 v48, v48, 0x3dd53b94, v138
	v_fmamk_f32 v49, v49, 0x3dd53b94, v138
	v_fmamk_f32 v50, v50, 0x3dd53b94, v138
	v_fmamk_f32 v51, v51, 0x3dd53b94, v138
	v_fmamk_f32 v52, v52, 0x3dd53b94, v138
	v_fmamk_f32 v53, v53, 0x3dd53b94, v138
	v_fmamk_f32 v54, v54, 0x3dd53b94, v138
	v_fmamk_f32 v55, v55, 0x3dd53b94, v138
	v_fmamk_f32 v56, v56, 0x3dd53b94, v138
	v_fmamk_f32 v57, v57, 0x3dd53b94, v138
	v_fmamk_f32 v58, v58, 0x3dd53b94, v138
	v_fmamk_f32 v59, v59, 0x3dd53b94, v138
	v_fmamk_f32 v60, v60, 0x3dd53b94, v138
	v_fmamk_f32 v61, v61, 0x3dd53b94, v138
	v_fmamk_f32 v62, v62, 0x3dd53b94, v138
	v_fmac_f32_e32 v165, 0x3dd53b94, v63
	s_mov_b32 s10, s27
	s_mov_b32 s11, s27
	v_mov_b64_e32 v[30:31], s[22:23]
	v_exp_f32_e32 v222, v48
	v_exp_f32_e32 v224, v49
	v_exp_f32_e32 v220, v50
	v_exp_f32_e32 v223, v51
	v_exp_f32_e32 v219, v52
	v_exp_f32_e32 v221, v53
	v_exp_f32_e32 v217, v54
	v_exp_f32_e32 v218, v55
	v_exp_f32_e32 v212, v56
	v_exp_f32_e32 v214, v57
	v_exp_f32_e32 v211, v58
	v_exp_f32_e32 v213, v59
	v_exp_f32_e32 v208, v60
	v_exp_f32_e32 v210, v61
	v_exp_f32_e32 v207, v62
	v_exp_f32_e32 v209, v165
	v_mov_b64_e32 v[16:17], s[8:9]
	s_waitcnt vmcnt(0)
	v_mov_b64_e32 v[28:29], s[20:21]
	v_mov_b64_e32 v[26:27], s[18:19]
	v_mov_b64_e32 v[24:25], s[16:17]
	v_mov_b64_e32 v[22:23], s[14:15]
	v_mov_b64_e32 v[20:21], s[12:13]
	v_mov_b64_e32 v[18:19], s[10:11]
	v_mov_b64_e32 v[46:47], v[30:31]
	v_mov_b64_e32 v[0:1], v[16:17]
	v_mov_b64_e32 v[62:63], v[30:31]
	v_mov_b64_e32 v[44:45], v[28:29]
	v_mov_b64_e32 v[42:43], v[26:27]
	v_mov_b64_e32 v[40:41], v[24:25]
	v_mov_b64_e32 v[38:39], v[22:23]
	v_mov_b64_e32 v[36:37], v[20:21]
	v_mov_b64_e32 v[34:35], v[18:19]
	v_mov_b64_e32 v[32:33], v[16:17]
	v_mov_b64_e32 v[2:3], v[18:19]
	v_mov_b64_e32 v[4:5], v[20:21]
	v_mov_b64_e32 v[6:7], v[22:23]
	v_mov_b64_e32 v[8:9], v[24:25]
	v_mov_b64_e32 v[10:11], v[26:27]
	v_mov_b64_e32 v[12:13], v[28:29]
	v_mov_b64_e32 v[14:15], v[30:31]
	s_add_i32 s10, s26, 0x80
	s_add_i32 s83, s26, 64
	s_sub_i32 s11, s65, 64
	v_pk_fma_f32 v[134:135], v[78:79], s[28:29], v[138:139] op_sel_hi:[1,0,0]
	v_pk_fma_f32 v[160:161], v[76:77], s[28:29], v[138:139] op_sel_hi:[1,0,0]
	v_pk_fma_f32 v[162:163], v[74:75], s[28:29], v[138:139] op_sel_hi:[1,0,0]
	v_pk_fma_f32 v[128:129], v[72:73], s[28:29], v[138:139] op_sel_hi:[1,0,0]
	v_pk_fma_f32 v[130:131], v[70:71], s[28:29], v[138:139] op_sel_hi:[1,0,0]
	v_pk_fma_f32 v[132:133], v[68:69], s[28:29], v[138:139] op_sel_hi:[1,0,0]
	v_pk_fma_f32 v[136:137], v[66:67], s[28:29], v[138:139] op_sel_hi:[1,0,0]
	v_pk_fma_f32 v[138:139], v[64:65], s[28:29], v[138:139] op_sel_hi:[1,0,0]
	v_cndmask_b32_e64 v197, v164, 1.0, vcc
	v_mov_b64_e32 v[60:61], v[28:29]
	v_mov_b64_e32 v[58:59], v[26:27]
	v_mov_b64_e32 v[56:57], v[24:25]
	v_mov_b64_e32 v[54:55], v[22:23]
	v_mov_b64_e32 v[52:53], v[20:21]
	v_mov_b64_e32 v[50:51], v[18:19]
	v_mov_b64_e32 v[48:49], v[16:17]
	s_waitcnt vmcnt(4)
	ds_write_b128 v175, v[80:83] offset:16384
	s_waitcnt vmcnt(3)
	ds_write_b128 v176, v[84:87] offset:16384
	s_waitcnt vmcnt(2)
	ds_write_b128 v177, v[88:91] offset:49152
	s_waitcnt vmcnt(1)
	ds_write_b128 v178, v[92:95] offset:49152
	s_waitcnt vmcnt(0)
	ds_write_b128 v196, v[200:203]
	s_waitcnt lgkmcnt(0)
	s_barrier
